# RG gate-GEMM epilogue hand-written with packed fp32 (v_pk_fma/add/mul_f32 on element pairs): phase probe 62.6 -> 55.7 us per execution
# baseline (speedup 1.0000x reference)
; __device__ __forceinline__ float bf_lo(unsigned w) { return __uint_as_float(w << 16); }
; __device__ __forceinline__ float bf_hi(unsigned w) { return __uint_as_float(w & 0xffff0000u); }
; __device__ __forceinline__ void store_bf16x8(bf16* p, const f32x4 v0, const f32x4 v1) { u32x4 w; w.x = cvt_pk_bf16(v0[0], v0[1]); w.y = cvt_pk_bf16(v0[2], v0[3]); w.z = cvt_pk_bf16(v1[0], v1[1]); w.w = cvt_pk_bf16(v1[2], v1[3]); *(u32x4*)p = w; }
; template <bool FP8>
; __device__ __forceinline__ void epilogue(const Desc& d, const Acc& acc, const Tile& u, LAS unsigned char* lds) {
;     ...
;         for (int n = 0; n < 2; ++n) { const f32x4 bx = *(const f32x4*)(gxb + ch0 + 4 * n), ba = *(const f32x4*)(gab + ch0 + 4 * n), lm = *(const f32x4*)(lam + ch0 + 4 * n);
; #pragma unroll
;             for (int j = 0; j < 4; ++j) { const float y = __expf(-lm[j]); sp[n][j] = -8.f * ((y < 0.03f) ? y * (1.f + y * (-0.5f + y * ((1.f / 3.f) - 0.25f * y))) : logf(1.f + y));
;                 sp2[n][j] = 2.f * L2E * sp[n][j]; nbx[n][j] = -L2E * bx[j]; nba[n][j] = -L2E * ba[j]; } }
; #pragma unroll
;         for (int ai = 0; ai < 2; ++ai) { u32x4 uw[4];
; #pragma unroll
;             for (int m = 0; m < 4; ++m) uw[m] = *(const u32x4*)(UF + (size_t)(row0 + ai * 128 + m * 16) * D + ch0);
; #pragma unroll
;             for (int m = 0; m < 4; ++m) { const size_t ro = (size_t)(row0 + ai * 128 + m * 16) * D + ch0;
;                 const float uf[2][4] = {{bf_lo(uw[m].x), bf_hi(uw[m].x), bf_lo(uw[m].y), bf_hi(uw[m].y)}, {bf_lo(uw[m].z), bf_hi(uw[m].z), bf_lo(uw[m].w), bf_hi(uw[m].w)}};
;                 f32x4 lo[2], bo[2];
; #pragma unroll
;                 for (int n = 0; n < 2; ++n)
; #pragma unroll
;                     for (int j = 0; j < 4; ++j) {
;                         const float it = __builtin_amdgcn_rcpf(1.f + __builtin_amdgcn_exp2f(__builtin_fmaf(acc[ai][0][m][n][j], -L2E, nbx[n][j])));
;                         const float rt = __builtin_amdgcn_rcpf(1.f + __builtin_amdgcn_exp2f(__builtin_fmaf(acc[ai][1][m][n][j], -L2E, nba[n][j])));
;                         const float em = 1.f - __builtin_amdgcn_exp2f(sp2[n][j] * rt);
;                         lo[n][j] = sp[n][j] * rt; bo[n][j] = __builtin_amdgcn_sqrtf(em) * (it * uf[n][j]); }
;                 store_bf16x8(la + ro, lo[0], lo[1]); store_bf16x8(bb + ro, bo[0], bo[1]); } }
.LBB0_554:
	s_andn2_saveexec_b64 s[6:7], s[6:7]
	v_fmamk_f32 v151, v154, 0xbe800000, v237
	v_fma_f32 v151, v154, v151, -0.5
	v_fma_f32 v151, v154, v151, 1.0
	v_mul_f32_e32 v151, v154, v151
	s_or_b64 exec, exec, s[6:7]
	s_waitcnt vmcnt(0)
	v_mul_f32_e32 v160, 0xbfb8aa3b, v132
	v_mul_f32_e32 v168, 0xbfb8aa3b, v136
	v_mul_f32_e32 v161, 0xbfb8aa3b, v133
	v_mul_f32_e32 v169, 0xbfb8aa3b, v137
	v_mul_f32_e32 v162, 0xbfb8aa3b, v134
	v_mul_f32_e32 v170, 0xbfb8aa3b, v138
	v_mul_f32_e32 v163, 0xbfb8aa3b, v135
	v_mul_f32_e32 v171, 0xbfb8aa3b, v139
	v_mul_f32_e32 v164, 0xbfb8aa3b, v140
	v_mul_f32_e32 v172, 0xbfb8aa3b, v144
	v_mul_f32_e32 v165, 0xbfb8aa3b, v141
	v_mul_f32_e32 v173, 0xbfb8aa3b, v145
	v_mul_f32_e32 v166, 0xbfb8aa3b, v142
	v_mul_f32_e32 v174, 0xbfb8aa3b, v146
	v_mul_f32_e32 v167, 0xbfb8aa3b, v143
	v_mul_f32_e32 v175, 0xbfb8aa3b, v147
	v_mul_f32_e32 v202, 0xc1000000, v66
	v_mul_f32_e32 v203, 0xc1000000, v156
	v_mul_f32_e32 v204, 0xc1000000, v157
	v_mul_f32_e32 v205, 0xc1000000, v158
	v_mul_f32_e32 v206, 0xc1000000, v148
	v_mul_f32_e32 v207, 0xc1000000, v149
	v_mul_f32_e32 v208, 0xc1000000, v150
	v_mul_f32_e32 v209, 0xc1000000, v151
	v_mul_f32_e32 v210, 0x4038aa3b, v202
	v_mul_f32_e32 v211, 0x4038aa3b, v203
	v_mul_f32_e32 v212, 0x4038aa3b, v204
	v_mul_f32_e32 v213, 0x4038aa3b, v205
	v_mul_f32_e32 v214, 0x4038aa3b, v206
	v_mul_f32_e32 v215, 0x4038aa3b, v207
	v_mul_f32_e32 v216, 0x4038aa3b, v208
	v_mul_f32_e32 v217, 0x4038aa3b, v209
	v_mov_b32_e32 v158, 0xbfb8aa3b
	v_mov_b32_e32 v159, 0xbfb8aa3b
	s_lshl_b32 s2, s2, 25
	s_add_u32 s42, s50, s2
	s_addc_u32 s43, s51, 0
	s_add_u32 s40, s72, s2
	s_addc_u32 s41, s73, 0
	v_lshl_add_u32 v195, s44, 8, v194
	v_lshlrev_b32_e32 v195, 10, v195
	v_add_u32_e32 v195, v195, v152
	v_lshlrev_b32_e32 v195, 1, v195
	v_mov_b32_e32 v197, v195
	global_load_dwordx4 v[132:135], v197, s[46:47]
	v_add_u32_e32 v197, 0x8000, v197
	global_load_dwordx4 v[136:139], v197, s[46:47]
	v_add_u32_e32 v197, 0x8000, v197
	global_load_dwordx4 v[140:143], v197, s[46:47]
	v_add_u32_e32 v197, 0x8000, v197
	global_load_dwordx4 v[144:147], v197, s[46:47]
	v_add_u32_e32 v197, 0x28000, v197
	s_waitcnt vmcnt(3)
	v_pk_fma_f32 v[120:121], v[120:121], v[158:159], v[168:169]
	v_pk_fma_f32 v[122:123], v[122:123], v[158:159], v[170:171]
	v_pk_fma_f32 v[128:129], v[128:129], v[158:159], v[160:161]
	v_pk_fma_f32 v[130:131], v[130:131], v[158:159], v[162:163]
	v_exp_f32_e32 v120, v120
	v_exp_f32_e32 v121, v121
	v_exp_f32_e32 v122, v122
	v_exp_f32_e32 v123, v123
	v_exp_f32_e32 v128, v128
	v_exp_f32_e32 v129, v129
	v_exp_f32_e32 v130, v130
	v_exp_f32_e32 v131, v131
	v_pk_add_f32 v[120:121], v[120:121], 1.0 op_sel_hi:[1,0]
	v_pk_add_f32 v[122:123], v[122:123], 1.0 op_sel_hi:[1,0]
	v_pk_add_f32 v[128:129], v[128:129], 1.0 op_sel_hi:[1,0]
	v_pk_add_f32 v[130:131], v[130:131], 1.0 op_sel_hi:[1,0]
	v_rcp_f32_e32 v120, v120
	v_rcp_f32_e32 v121, v121
	v_rcp_f32_e32 v122, v122
	v_rcp_f32_e32 v123, v123
	v_rcp_f32_e32 v128, v128
	v_rcp_f32_e32 v129, v129
	v_rcp_f32_e32 v130, v130
	v_rcp_f32_e32 v131, v131
	v_pk_mul_f32 v[154:155], v[120:121], v[210:211]
	v_pk_mul_f32 v[156:157], v[122:123], v[212:213]
	v_exp_f32_e32 v154, v154
	v_exp_f32_e32 v155, v155
	v_exp_f32_e32 v156, v156
	v_exp_f32_e32 v157, v157
	v_lshlrev_b32_e32 v224, 16, v132
	v_and_b32_e32 v225, 0xffff0000, v132
	v_lshlrev_b32_e32 v226, 16, v133
	v_and_b32_e32 v227, 0xffff0000, v133
	v_pk_add_f32 v[154:155], v[154:155], 1.0 op_sel_hi:[1,0] neg_lo:[1,0] neg_hi:[1,0]
	v_pk_add_f32 v[156:157], v[156:157], 1.0 op_sel_hi:[1,0] neg_lo:[1,0] neg_hi:[1,0]
	v_sqrt_f32_e32 v154, v154
	v_sqrt_f32_e32 v155, v155
	v_sqrt_f32_e32 v156, v156
	v_sqrt_f32_e32 v157, v157
	v_pk_mul_f32 v[128:129], v[128:129], v[224:225]
	v_pk_mul_f32 v[130:131], v[130:131], v[226:227]
	v_pk_mul_f32 v[120:121], v[120:121], v[202:203]
	v_pk_mul_f32 v[122:123], v[122:123], v[204:205]
	v_pk_mul_f32 v[128:129], v[154:155], v[128:129]
	v_pk_mul_f32 v[130:131], v[156:157], v[130:131]
	v_cvt_pk_bf16_f32 v148, v120, v121
	v_cvt_pk_bf16_f32 v176, v128, v129
	v_cvt_pk_bf16_f32 v149, v122, v123
	v_cvt_pk_bf16_f32 v177, v130, v131
	v_pk_fma_f32 v[116:117], v[116:117], v[158:159], v[172:173]
	v_pk_fma_f32 v[118:119], v[118:119], v[158:159], v[174:175]
	v_pk_fma_f32 v[124:125], v[124:125], v[158:159], v[164:165]
	v_pk_fma_f32 v[126:127], v[126:127], v[158:159], v[166:167]
	v_exp_f32_e32 v116, v116
	v_exp_f32_e32 v117, v117
	v_exp_f32_e32 v118, v118
	v_exp_f32_e32 v119, v119
	v_exp_f32_e32 v124, v124
	v_exp_f32_e32 v125, v125
	v_exp_f32_e32 v126, v126
	v_exp_f32_e32 v127, v127
	v_pk_add_f32 v[116:117], v[116:117], 1.0 op_sel_hi:[1,0]
	v_pk_add_f32 v[118:119], v[118:119], 1.0 op_sel_hi:[1,0]
	v_pk_add_f32 v[124:125], v[124:125], 1.0 op_sel_hi:[1,0]
	v_pk_add_f32 v[126:127], v[126:127], 1.0 op_sel_hi:[1,0]
	v_rcp_f32_e32 v116, v116
	v_rcp_f32_e32 v117, v117
	v_rcp_f32_e32 v118, v118
	v_rcp_f32_e32 v119, v119
	v_rcp_f32_e32 v124, v124
	v_rcp_f32_e32 v125, v125
	v_rcp_f32_e32 v126, v126
	v_rcp_f32_e32 v127, v127
	v_pk_mul_f32 v[154:155], v[116:117], v[214:215]
	v_pk_mul_f32 v[156:157], v[118:119], v[216:217]
	v_exp_f32_e32 v154, v154
	v_exp_f32_e32 v155, v155
	v_exp_f32_e32 v156, v156
	v_exp_f32_e32 v157, v157
	v_lshlrev_b32_e32 v224, 16, v134
	v_and_b32_e32 v225, 0xffff0000, v134
	v_lshlrev_b32_e32 v226, 16, v135
	v_and_b32_e32 v227, 0xffff0000, v135
	v_pk_add_f32 v[154:155], v[154:155], 1.0 op_sel_hi:[1,0] neg_lo:[1,0] neg_hi:[1,0]
	v_pk_add_f32 v[156:157], v[156:157], 1.0 op_sel_hi:[1,0] neg_lo:[1,0] neg_hi:[1,0]
	v_sqrt_f32_e32 v154, v154
	v_sqrt_f32_e32 v155, v155
	v_sqrt_f32_e32 v156, v156
	v_sqrt_f32_e32 v157, v157
	v_pk_mul_f32 v[124:125], v[124:125], v[224:225]
	v_pk_mul_f32 v[126:127], v[126:127], v[226:227]
	v_pk_mul_f32 v[116:117], v[116:117], v[206:207]
	v_pk_mul_f32 v[118:119], v[118:119], v[208:209]
	v_pk_mul_f32 v[124:125], v[154:155], v[124:125]
	v_pk_mul_f32 v[126:127], v[156:157], v[126:127]
	v_cvt_pk_bf16_f32 v150, v116, v117
	v_cvt_pk_bf16_f32 v178, v124, v125
	v_cvt_pk_bf16_f32 v151, v118, v119
	v_cvt_pk_bf16_f32 v179, v126, v127
	global_load_dwordx4 v[128:131], v197, s[46:47]
	v_add_u32_e32 v197, 0x8000, v197
	global_load_dwordx4 v[124:127], v197, s[46:47]
	v_add_u32_e32 v197, 0x8000, v197
	global_load_dwordx4 v[120:123], v197, s[46:47]
	v_add_u32_e32 v197, 0x8000, v197
	global_load_dwordx4 v[116:119], v197, s[46:47]
	global_store_dwordx4 v195, v[148:151], s[42:43]
	global_store_dwordx4 v195, v[176:179], s[40:41]
	v_add_u32_e32 v195, 0x8000, v195
	s_waitcnt vmcnt(8)
; __device__ __forceinline__ float bf_lo(unsigned w) { return __uint_as_float(w << 16); }
; __device__ __forceinline__ float bf_hi(unsigned w) { return __uint_as_float(w & 0xffff0000u); }
; __device__ __forceinline__ void store_bf16x8(bf16* p, const f32x4 v0, const f32x4 v1) { u32x4 w; w.x = cvt_pk_bf16(v0[0], v0[1]); w.y = cvt_pk_bf16(v0[2], v0[3]); w.z = cvt_pk_bf16(v1[0], v1[1]); w.w = cvt_pk_bf16(v1[2], v1[3]); *(u32x4*)p = w; }
; template <bool FP8>
; __device__ __forceinline__ void epilogue(const Desc& d, const Acc& acc, const Tile& u, LAS unsigned char* lds) {
;     ...
;         for (int ai = 0; ai < 2; ++ai) { u32x4 uw[4];
; #pragma unroll
;             for (int m = 0; m < 4; ++m) uw[m] = *(const u32x4*)(UF + (size_t)(row0 + ai * 128 + m * 16) * D + ch0);
; #pragma unroll
;             for (int m = 0; m < 4; ++m) { const size_t ro = (size_t)(row0 + ai * 128 + m * 16) * D + ch0;
;                 const float uf[2][4] = {{bf_lo(uw[m].x), bf_hi(uw[m].x), bf_lo(uw[m].y), bf_hi(uw[m].y)}, {bf_lo(uw[m].z), bf_hi(uw[m].z), bf_lo(uw[m].w), bf_hi(uw[m].w)}};
;                 f32x4 lo[2], bo[2];
; #pragma unroll
;                 for (int n = 0; n < 2; ++n)
; #pragma unroll
;                     for (int j = 0; j < 4; ++j) {
;                         const float it = __builtin_amdgcn_rcpf(1.f + __builtin_amdgcn_exp2f(__builtin_fmaf(acc[ai][0][m][n][j], -L2E, nbx[n][j])));
;                         const float rt = __builtin_amdgcn_rcpf(1.f + __builtin_amdgcn_exp2f(__builtin_fmaf(acc[ai][1][m][n][j], -L2E, nba[n][j])));
;                         const float em = 1.f - __builtin_amdgcn_exp2f(sp2[n][j] * rt);
;                         lo[n][j] = sp[n][j] * rt; bo[n][j] = __builtin_amdgcn_sqrtf(em) * (it * uf[n][j]); }
;                 store_bf16x8(la + ro, lo[0], lo[1]); store_bf16x8(bb + ro, bo[0], bo[1]); } }
	v_pk_fma_f32 v[104:105], v[104:105], v[158:159], v[168:169]
	v_pk_fma_f32 v[106:107], v[106:107], v[158:159], v[170:171]
	v_pk_fma_f32 v[112:113], v[112:113], v[158:159], v[160:161]
	v_pk_fma_f32 v[114:115], v[114:115], v[158:159], v[162:163]
	v_exp_f32_e32 v104, v104
	v_exp_f32_e32 v105, v105
	v_exp_f32_e32 v106, v106
	v_exp_f32_e32 v107, v107
	v_exp_f32_e32 v112, v112
	v_exp_f32_e32 v113, v113
	v_exp_f32_e32 v114, v114
	v_exp_f32_e32 v115, v115
	v_pk_add_f32 v[104:105], v[104:105], 1.0 op_sel_hi:[1,0]
	v_pk_add_f32 v[106:107], v[106:107], 1.0 op_sel_hi:[1,0]
	v_pk_add_f32 v[112:113], v[112:113], 1.0 op_sel_hi:[1,0]
	v_pk_add_f32 v[114:115], v[114:115], 1.0 op_sel_hi:[1,0]
	v_rcp_f32_e32 v104, v104
	v_rcp_f32_e32 v105, v105
	v_rcp_f32_e32 v106, v106
	v_rcp_f32_e32 v107, v107
	v_rcp_f32_e32 v112, v112
	v_rcp_f32_e32 v113, v113
	v_rcp_f32_e32 v114, v114
	v_rcp_f32_e32 v115, v115
	v_pk_mul_f32 v[154:155], v[104:105], v[210:211]
	v_pk_mul_f32 v[156:157], v[106:107], v[212:213]
	v_exp_f32_e32 v154, v154
	v_exp_f32_e32 v155, v155
	v_exp_f32_e32 v156, v156
	v_exp_f32_e32 v157, v157
	v_lshlrev_b32_e32 v224, 16, v136
	v_and_b32_e32 v225, 0xffff0000, v136
	v_lshlrev_b32_e32 v226, 16, v137
	v_and_b32_e32 v227, 0xffff0000, v137
	v_pk_add_f32 v[154:155], v[154:155], 1.0 op_sel_hi:[1,0] neg_lo:[1,0] neg_hi:[1,0]
	v_pk_add_f32 v[156:157], v[156:157], 1.0 op_sel_hi:[1,0] neg_lo:[1,0] neg_hi:[1,0]
	v_sqrt_f32_e32 v154, v154
	v_sqrt_f32_e32 v155, v155
	v_sqrt_f32_e32 v156, v156
	v_sqrt_f32_e32 v157, v157
	v_pk_mul_f32 v[112:113], v[112:113], v[224:225]
	v_pk_mul_f32 v[114:115], v[114:115], v[226:227]
	v_pk_mul_f32 v[104:105], v[104:105], v[202:203]
	v_pk_mul_f32 v[106:107], v[106:107], v[204:205]
	v_pk_mul_f32 v[112:113], v[154:155], v[112:113]
	v_pk_mul_f32 v[114:115], v[156:157], v[114:115]
	v_cvt_pk_bf16_f32 v148, v104, v105
	v_cvt_pk_bf16_f32 v176, v112, v113
	v_cvt_pk_bf16_f32 v149, v106, v107
	v_cvt_pk_bf16_f32 v177, v114, v115
	v_pk_fma_f32 v[100:101], v[100:101], v[158:159], v[172:173]
	v_pk_fma_f32 v[102:103], v[102:103], v[158:159], v[174:175]
	v_pk_fma_f32 v[108:109], v[108:109], v[158:159], v[164:165]
	v_pk_fma_f32 v[110:111], v[110:111], v[158:159], v[166:167]
	v_exp_f32_e32 v100, v100
	v_exp_f32_e32 v101, v101
	v_exp_f32_e32 v102, v102
	v_exp_f32_e32 v103, v103
	v_exp_f32_e32 v108, v108
	v_exp_f32_e32 v109, v109
	v_exp_f32_e32 v110, v110
	v_exp_f32_e32 v111, v111
	v_pk_add_f32 v[100:101], v[100:101], 1.0 op_sel_hi:[1,0]
	v_pk_add_f32 v[102:103], v[102:103], 1.0 op_sel_hi:[1,0]
	v_pk_add_f32 v[108:109], v[108:109], 1.0 op_sel_hi:[1,0]
	v_pk_add_f32 v[110:111], v[110:111], 1.0 op_sel_hi:[1,0]
	v_rcp_f32_e32 v100, v100
	v_rcp_f32_e32 v101, v101
	v_rcp_f32_e32 v102, v102
	v_rcp_f32_e32 v103, v103
	v_rcp_f32_e32 v108, v108
	v_rcp_f32_e32 v109, v109
	v_rcp_f32_e32 v110, v110
	v_rcp_f32_e32 v111, v111
	v_pk_mul_f32 v[154:155], v[100:101], v[214:215]
	v_pk_mul_f32 v[156:157], v[102:103], v[216:217]
	v_exp_f32_e32 v154, v154
	v_exp_f32_e32 v155, v155
	v_exp_f32_e32 v156, v156
	v_exp_f32_e32 v157, v157
	v_lshlrev_b32_e32 v224, 16, v138
	v_and_b32_e32 v225, 0xffff0000, v138
	v_lshlrev_b32_e32 v226, 16, v139
	v_and_b32_e32 v227, 0xffff0000, v139
	v_pk_add_f32 v[154:155], v[154:155], 1.0 op_sel_hi:[1,0] neg_lo:[1,0] neg_hi:[1,0]
	v_pk_add_f32 v[156:157], v[156:157], 1.0 op_sel_hi:[1,0] neg_lo:[1,0] neg_hi:[1,0]
	v_sqrt_f32_e32 v154, v154
	v_sqrt_f32_e32 v155, v155
	v_sqrt_f32_e32 v156, v156
	v_sqrt_f32_e32 v157, v157
	v_pk_mul_f32 v[108:109], v[108:109], v[224:225]
	v_pk_mul_f32 v[110:111], v[110:111], v[226:227]
	v_pk_mul_f32 v[100:101], v[100:101], v[206:207]
	v_pk_mul_f32 v[102:103], v[102:103], v[208:209]
	v_pk_mul_f32 v[108:109], v[154:155], v[108:109]
	v_pk_mul_f32 v[110:111], v[156:157], v[110:111]
	v_cvt_pk_bf16_f32 v150, v100, v101
	v_cvt_pk_bf16_f32 v178, v108, v109
	v_cvt_pk_bf16_f32 v151, v102, v103
	v_cvt_pk_bf16_f32 v179, v110, v111
	global_store_dwordx4 v195, v[148:151], s[42:43]
	global_store_dwordx4 v195, v[176:179], s[40:41]
	v_add_u32_e32 v195, 0x8000, v195
	s_waitcnt vmcnt(9)
	v_pk_fma_f32 v[88:89], v[88:89], v[158:159], v[168:169]
	v_pk_fma_f32 v[90:91], v[90:91], v[158:159], v[170:171]
	v_pk_fma_f32 v[96:97], v[96:97], v[158:159], v[160:161]
	v_pk_fma_f32 v[98:99], v[98:99], v[158:159], v[162:163]
	v_exp_f32_e32 v88, v88
	v_exp_f32_e32 v89, v89
	v_exp_f32_e32 v90, v90
	v_exp_f32_e32 v91, v91
	v_exp_f32_e32 v96, v96
	v_exp_f32_e32 v97, v97
	v_exp_f32_e32 v98, v98
	v_exp_f32_e32 v99, v99
	v_pk_add_f32 v[88:89], v[88:89], 1.0 op_sel_hi:[1,0]
	v_pk_add_f32 v[90:91], v[90:91], 1.0 op_sel_hi:[1,0]
	v_pk_add_f32 v[96:97], v[96:97], 1.0 op_sel_hi:[1,0]
	v_pk_add_f32 v[98:99], v[98:99], 1.0 op_sel_hi:[1,0]
	v_rcp_f32_e32 v88, v88
	v_rcp_f32_e32 v89, v89
	v_rcp_f32_e32 v90, v90
	v_rcp_f32_e32 v91, v91
	v_rcp_f32_e32 v96, v96
	v_rcp_f32_e32 v97, v97
	v_rcp_f32_e32 v98, v98
	v_rcp_f32_e32 v99, v99
	v_pk_mul_f32 v[154:155], v[88:89], v[210:211]
	v_pk_mul_f32 v[156:157], v[90:91], v[212:213]
	v_exp_f32_e32 v154, v154
	v_exp_f32_e32 v155, v155
	v_exp_f32_e32 v156, v156
	v_exp_f32_e32 v157, v157
	v_lshlrev_b32_e32 v224, 16, v140
	v_and_b32_e32 v225, 0xffff0000, v140
	v_lshlrev_b32_e32 v226, 16, v141
	v_and_b32_e32 v227, 0xffff0000, v141
	v_pk_add_f32 v[154:155], v[154:155], 1.0 op_sel_hi:[1,0] neg_lo:[1,0] neg_hi:[1,0]
	v_pk_add_f32 v[156:157], v[156:157], 1.0 op_sel_hi:[1,0] neg_lo:[1,0] neg_hi:[1,0]
	v_sqrt_f32_e32 v154, v154
	v_sqrt_f32_e32 v155, v155
	v_sqrt_f32_e32 v156, v156
	v_sqrt_f32_e32 v157, v157
	v_pk_mul_f32 v[96:97], v[96:97], v[224:225]
	v_pk_mul_f32 v[98:99], v[98:99], v[226:227]
	v_pk_mul_f32 v[88:89], v[88:89], v[202:203]
; __device__ __forceinline__ float bf_lo(unsigned w) { return __uint_as_float(w << 16); }
; __device__ __forceinline__ float bf_hi(unsigned w) { return __uint_as_float(w & 0xffff0000u); }
; __device__ __forceinline__ void store_bf16x8(bf16* p, const f32x4 v0, const f32x4 v1) { u32x4 w; w.x = cvt_pk_bf16(v0[0], v0[1]); w.y = cvt_pk_bf16(v0[2], v0[3]); w.z = cvt_pk_bf16(v1[0], v1[1]); w.w = cvt_pk_bf16(v1[2], v1[3]); *(u32x4*)p = w; }
; template <bool FP8>
; __device__ __forceinline__ void epilogue(const Desc& d, const Acc& acc, const Tile& u, LAS unsigned char* lds) {
;     ...
;         for (int ai = 0; ai < 2; ++ai) { u32x4 uw[4];
; #pragma unroll
;             for (int m = 0; m < 4; ++m) uw[m] = *(const u32x4*)(UF + (size_t)(row0 + ai * 128 + m * 16) * D + ch0);
; #pragma unroll
;             for (int m = 0; m < 4; ++m) { const size_t ro = (size_t)(row0 + ai * 128 + m * 16) * D + ch0;
;                 const float uf[2][4] = {{bf_lo(uw[m].x), bf_hi(uw[m].x), bf_lo(uw[m].y), bf_hi(uw[m].y)}, {bf_lo(uw[m].z), bf_hi(uw[m].z), bf_lo(uw[m].w), bf_hi(uw[m].w)}};
;                 f32x4 lo[2], bo[2];
; #pragma unroll
;                 for (int n = 0; n < 2; ++n)
; #pragma unroll
;                     for (int j = 0; j < 4; ++j) {
;                         const float it = __builtin_amdgcn_rcpf(1.f + __builtin_amdgcn_exp2f(__builtin_fmaf(acc[ai][0][m][n][j], -L2E, nbx[n][j])));
;                         const float rt = __builtin_amdgcn_rcpf(1.f + __builtin_amdgcn_exp2f(__builtin_fmaf(acc[ai][1][m][n][j], -L2E, nba[n][j])));
;                         const float em = 1.f - __builtin_amdgcn_exp2f(sp2[n][j] * rt);
;                         lo[n][j] = sp[n][j] * rt; bo[n][j] = __builtin_amdgcn_sqrtf(em) * (it * uf[n][j]); }
;                 store_bf16x8(la + ro, lo[0], lo[1]); store_bf16x8(bb + ro, bo[0], bo[1]); } }
	v_pk_mul_f32 v[90:91], v[90:91], v[204:205]
	v_pk_mul_f32 v[96:97], v[154:155], v[96:97]
	v_pk_mul_f32 v[98:99], v[156:157], v[98:99]
	v_cvt_pk_bf16_f32 v148, v88, v89
	v_cvt_pk_bf16_f32 v176, v96, v97
	v_cvt_pk_bf16_f32 v149, v90, v91
	v_cvt_pk_bf16_f32 v177, v98, v99
	v_pk_fma_f32 v[84:85], v[84:85], v[158:159], v[172:173]
	v_pk_fma_f32 v[86:87], v[86:87], v[158:159], v[174:175]
	v_pk_fma_f32 v[92:93], v[92:93], v[158:159], v[164:165]
	v_pk_fma_f32 v[94:95], v[94:95], v[158:159], v[166:167]
	v_exp_f32_e32 v84, v84
	v_exp_f32_e32 v85, v85
	v_exp_f32_e32 v86, v86
	v_exp_f32_e32 v87, v87
	v_exp_f32_e32 v92, v92
	v_exp_f32_e32 v93, v93
	v_exp_f32_e32 v94, v94
	v_exp_f32_e32 v95, v95
	v_pk_add_f32 v[84:85], v[84:85], 1.0 op_sel_hi:[1,0]
	v_pk_add_f32 v[86:87], v[86:87], 1.0 op_sel_hi:[1,0]
	v_pk_add_f32 v[92:93], v[92:93], 1.0 op_sel_hi:[1,0]
	v_pk_add_f32 v[94:95], v[94:95], 1.0 op_sel_hi:[1,0]
	v_rcp_f32_e32 v84, v84
	v_rcp_f32_e32 v85, v85
	v_rcp_f32_e32 v86, v86
	v_rcp_f32_e32 v87, v87
	v_rcp_f32_e32 v92, v92
	v_rcp_f32_e32 v93, v93
	v_rcp_f32_e32 v94, v94
	v_rcp_f32_e32 v95, v95
	v_pk_mul_f32 v[154:155], v[84:85], v[214:215]
	v_pk_mul_f32 v[156:157], v[86:87], v[216:217]
	v_exp_f32_e32 v154, v154
	v_exp_f32_e32 v155, v155
	v_exp_f32_e32 v156, v156
	v_exp_f32_e32 v157, v157
	v_lshlrev_b32_e32 v224, 16, v142
	v_and_b32_e32 v225, 0xffff0000, v142
	v_lshlrev_b32_e32 v226, 16, v143
	v_and_b32_e32 v227, 0xffff0000, v143
	v_pk_add_f32 v[154:155], v[154:155], 1.0 op_sel_hi:[1,0] neg_lo:[1,0] neg_hi:[1,0]
	v_pk_add_f32 v[156:157], v[156:157], 1.0 op_sel_hi:[1,0] neg_lo:[1,0] neg_hi:[1,0]
	v_sqrt_f32_e32 v154, v154
	v_sqrt_f32_e32 v155, v155
	v_sqrt_f32_e32 v156, v156
	v_sqrt_f32_e32 v157, v157
	v_pk_mul_f32 v[92:93], v[92:93], v[224:225]
	v_pk_mul_f32 v[94:95], v[94:95], v[226:227]
	v_pk_mul_f32 v[84:85], v[84:85], v[206:207]
	v_pk_mul_f32 v[86:87], v[86:87], v[208:209]
	v_pk_mul_f32 v[92:93], v[154:155], v[92:93]
	v_pk_mul_f32 v[94:95], v[156:157], v[94:95]
	v_cvt_pk_bf16_f32 v150, v84, v85
	v_cvt_pk_bf16_f32 v178, v92, v93
	v_cvt_pk_bf16_f32 v151, v86, v87
	v_cvt_pk_bf16_f32 v179, v94, v95
	global_store_dwordx4 v195, v[148:151], s[42:43]
	global_store_dwordx4 v195, v[176:179], s[40:41]
	v_add_u32_e32 v195, 0x8000, v195
	s_waitcnt vmcnt(10)
	v_pk_fma_f32 v[72:73], v[72:73], v[158:159], v[168:169]
	v_pk_fma_f32 v[74:75], v[74:75], v[158:159], v[170:171]
	v_pk_fma_f32 v[80:81], v[80:81], v[158:159], v[160:161]
	v_pk_fma_f32 v[82:83], v[82:83], v[158:159], v[162:163]
	v_exp_f32_e32 v72, v72
	v_exp_f32_e32 v73, v73
	v_exp_f32_e32 v74, v74
	v_exp_f32_e32 v75, v75
	v_exp_f32_e32 v80, v80
	v_exp_f32_e32 v81, v81
	v_exp_f32_e32 v82, v82
	v_exp_f32_e32 v83, v83
	v_pk_add_f32 v[72:73], v[72:73], 1.0 op_sel_hi:[1,0]
	v_pk_add_f32 v[74:75], v[74:75], 1.0 op_sel_hi:[1,0]
	v_pk_add_f32 v[80:81], v[80:81], 1.0 op_sel_hi:[1,0]
	v_pk_add_f32 v[82:83], v[82:83], 1.0 op_sel_hi:[1,0]
	v_rcp_f32_e32 v72, v72
	v_rcp_f32_e32 v73, v73
	v_rcp_f32_e32 v74, v74
	v_rcp_f32_e32 v75, v75
	v_rcp_f32_e32 v80, v80
	v_rcp_f32_e32 v81, v81
	v_rcp_f32_e32 v82, v82
	v_rcp_f32_e32 v83, v83
	v_pk_mul_f32 v[154:155], v[72:73], v[210:211]
	v_pk_mul_f32 v[156:157], v[74:75], v[212:213]
	v_exp_f32_e32 v154, v154
	v_exp_f32_e32 v155, v155
	v_exp_f32_e32 v156, v156
	v_exp_f32_e32 v157, v157
	v_lshlrev_b32_e32 v224, 16, v144
	v_and_b32_e32 v225, 0xffff0000, v144
	v_lshlrev_b32_e32 v226, 16, v145
	v_and_b32_e32 v227, 0xffff0000, v145
	v_pk_add_f32 v[154:155], v[154:155], 1.0 op_sel_hi:[1,0] neg_lo:[1,0] neg_hi:[1,0]
	v_pk_add_f32 v[156:157], v[156:157], 1.0 op_sel_hi:[1,0] neg_lo:[1,0] neg_hi:[1,0]
	v_sqrt_f32_e32 v154, v154
	v_sqrt_f32_e32 v155, v155
	v_sqrt_f32_e32 v156, v156
	v_sqrt_f32_e32 v157, v157
	v_pk_mul_f32 v[80:81], v[80:81], v[224:225]
	v_pk_mul_f32 v[82:83], v[82:83], v[226:227]
	v_pk_mul_f32 v[72:73], v[72:73], v[202:203]
	v_pk_mul_f32 v[74:75], v[74:75], v[204:205]
	v_pk_mul_f32 v[80:81], v[154:155], v[80:81]
	v_pk_mul_f32 v[82:83], v[156:157], v[82:83]
	v_cvt_pk_bf16_f32 v148, v72, v73
	v_cvt_pk_bf16_f32 v176, v80, v81
	v_cvt_pk_bf16_f32 v149, v74, v75
	v_cvt_pk_bf16_f32 v177, v82, v83
	v_pk_fma_f32 v[68:69], v[68:69], v[158:159], v[172:173]
	v_pk_fma_f32 v[70:71], v[70:71], v[158:159], v[174:175]
	v_pk_fma_f32 v[76:77], v[76:77], v[158:159], v[164:165]
	v_pk_fma_f32 v[78:79], v[78:79], v[158:159], v[166:167]
	v_exp_f32_e32 v68, v68
	v_exp_f32_e32 v69, v69
	v_exp_f32_e32 v70, v70
	v_exp_f32_e32 v71, v71
	v_exp_f32_e32 v76, v76
	v_exp_f32_e32 v77, v77
	v_exp_f32_e32 v78, v78
	v_exp_f32_e32 v79, v79
	v_pk_add_f32 v[68:69], v[68:69], 1.0 op_sel_hi:[1,0]
	v_pk_add_f32 v[70:71], v[70:71], 1.0 op_sel_hi:[1,0]
	v_pk_add_f32 v[76:77], v[76:77], 1.0 op_sel_hi:[1,0]
	v_pk_add_f32 v[78:79], v[78:79], 1.0 op_sel_hi:[1,0]
	v_rcp_f32_e32 v68, v68
	v_rcp_f32_e32 v69, v69
	v_rcp_f32_e32 v70, v70
	v_rcp_f32_e32 v71, v71
	v_rcp_f32_e32 v76, v76
	v_rcp_f32_e32 v77, v77
	v_rcp_f32_e32 v78, v78
	v_rcp_f32_e32 v79, v79
	v_pk_mul_f32 v[154:155], v[68:69], v[214:215]
	v_pk_mul_f32 v[156:157], v[70:71], v[216:217]
	v_exp_f32_e32 v154, v154
	v_exp_f32_e32 v155, v155
	v_exp_f32_e32 v156, v156
	v_exp_f32_e32 v157, v157
	v_lshlrev_b32_e32 v224, 16, v146
	v_and_b32_e32 v225, 0xffff0000, v146
	v_lshlrev_b32_e32 v226, 16, v147
	v_and_b32_e32 v227, 0xffff0000, v147
	v_pk_add_f32 v[154:155], v[154:155], 1.0 op_sel_hi:[1,0] neg_lo:[1,0] neg_hi:[1,0]
	v_pk_add_f32 v[156:157], v[156:157], 1.0 op_sel_hi:[1,0] neg_lo:[1,0] neg_hi:[1,0]
	v_sqrt_f32_e32 v154, v154
	v_sqrt_f32_e32 v155, v155
	v_sqrt_f32_e32 v156, v156
	v_sqrt_f32_e32 v157, v157
	v_pk_mul_f32 v[76:77], v[76:77], v[224:225]
	v_pk_mul_f32 v[78:79], v[78:79], v[226:227]
	v_pk_mul_f32 v[68:69], v[68:69], v[206:207]
	v_pk_mul_f32 v[70:71], v[70:71], v[208:209]
	v_pk_mul_f32 v[76:77], v[154:155], v[76:77]
	v_pk_mul_f32 v[78:79], v[156:157], v[78:79]
	v_cvt_pk_bf16_f32 v150, v68, v69
	v_cvt_pk_bf16_f32 v178, v76, v77
	v_cvt_pk_bf16_f32 v151, v70, v71
	v_cvt_pk_bf16_f32 v179, v78, v79
	global_store_dwordx4 v195, v[148:151], s[42:43]
	global_store_dwordx4 v195, v[176:179], s[40:41]
	v_add_u32_e32 v195, 0x28000, v195
	s_waitcnt vmcnt(11)
; __device__ __forceinline__ float bf_lo(unsigned w) { return __uint_as_float(w << 16); }
; __device__ __forceinline__ float bf_hi(unsigned w) { return __uint_as_float(w & 0xffff0000u); }
; __device__ __forceinline__ void store_bf16x8(bf16* p, const f32x4 v0, const f32x4 v1) { u32x4 w; w.x = cvt_pk_bf16(v0[0], v0[1]); w.y = cvt_pk_bf16(v0[2], v0[3]); w.z = cvt_pk_bf16(v1[0], v1[1]); w.w = cvt_pk_bf16(v1[2], v1[3]); *(u32x4*)p = w; }
; template <bool FP8>
; __device__ __forceinline__ void epilogue(const Desc& d, const Acc& acc, const Tile& u, LAS unsigned char* lds) {
;     ...
;             for (int m = 0; m < 4; ++m) { const size_t ro = (size_t)(row0 + ai * 128 + m * 16) * D + ch0;
;                 const float uf[2][4] = {{bf_lo(uw[m].x), bf_hi(uw[m].x), bf_lo(uw[m].y), bf_hi(uw[m].y)}, {bf_lo(uw[m].z), bf_hi(uw[m].z), bf_lo(uw[m].w), bf_hi(uw[m].w)}};
;                 f32x4 lo[2], bo[2];
; #pragma unroll
;                 for (int n = 0; n < 2; ++n)
; #pragma unroll
;                     for (int j = 0; j < 4; ++j) {
;                         const float it = __builtin_amdgcn_rcpf(1.f + __builtin_amdgcn_exp2f(__builtin_fmaf(acc[ai][0][m][n][j], -L2E, nbx[n][j])));
;                         const float rt = __builtin_amdgcn_rcpf(1.f + __builtin_amdgcn_exp2f(__builtin_fmaf(acc[ai][1][m][n][j], -L2E, nba[n][j])));
;                         const float em = 1.f - __builtin_amdgcn_exp2f(sp2[n][j] * rt);
;                         lo[n][j] = sp[n][j] * rt; bo[n][j] = __builtin_amdgcn_sqrtf(em) * (it * uf[n][j]); }
;                 store_bf16x8(la + ro, lo[0], lo[1]); store_bf16x8(bb + ro, bo[0], bo[1]); } }
	v_pk_fma_f32 v[54:55], v[54:55], v[158:159], v[168:169]
	v_pk_fma_f32 v[56:57], v[56:57], v[158:159], v[170:171]
	v_pk_fma_f32 v[62:63], v[62:63], v[158:159], v[160:161]
	v_pk_fma_f32 v[64:65], v[64:65], v[158:159], v[162:163]
	v_exp_f32_e32 v54, v54
	v_exp_f32_e32 v55, v55
	v_exp_f32_e32 v56, v56
	v_exp_f32_e32 v57, v57
	v_exp_f32_e32 v62, v62
	v_exp_f32_e32 v63, v63
	v_exp_f32_e32 v64, v64
	v_exp_f32_e32 v65, v65
	v_pk_add_f32 v[54:55], v[54:55], 1.0 op_sel_hi:[1,0]
	v_pk_add_f32 v[56:57], v[56:57], 1.0 op_sel_hi:[1,0]
	v_pk_add_f32 v[62:63], v[62:63], 1.0 op_sel_hi:[1,0]
	v_pk_add_f32 v[64:65], v[64:65], 1.0 op_sel_hi:[1,0]
	v_rcp_f32_e32 v54, v54
	v_rcp_f32_e32 v55, v55
	v_rcp_f32_e32 v56, v56
	v_rcp_f32_e32 v57, v57
	v_rcp_f32_e32 v62, v62
	v_rcp_f32_e32 v63, v63
	v_rcp_f32_e32 v64, v64
	v_rcp_f32_e32 v65, v65
	v_pk_mul_f32 v[154:155], v[54:55], v[210:211]
	v_pk_mul_f32 v[156:157], v[56:57], v[212:213]
	v_exp_f32_e32 v154, v154
	v_exp_f32_e32 v155, v155
	v_exp_f32_e32 v156, v156
	v_exp_f32_e32 v157, v157
	v_lshlrev_b32_e32 v224, 16, v128
	v_and_b32_e32 v225, 0xffff0000, v128
	v_lshlrev_b32_e32 v226, 16, v129
	v_and_b32_e32 v227, 0xffff0000, v129
	v_pk_add_f32 v[154:155], v[154:155], 1.0 op_sel_hi:[1,0] neg_lo:[1,0] neg_hi:[1,0]
	v_pk_add_f32 v[156:157], v[156:157], 1.0 op_sel_hi:[1,0] neg_lo:[1,0] neg_hi:[1,0]
	v_sqrt_f32_e32 v154, v154
	v_sqrt_f32_e32 v155, v155
	v_sqrt_f32_e32 v156, v156
	v_sqrt_f32_e32 v157, v157
	v_pk_mul_f32 v[62:63], v[62:63], v[224:225]
	v_pk_mul_f32 v[64:65], v[64:65], v[226:227]
	v_pk_mul_f32 v[54:55], v[54:55], v[202:203]
	v_pk_mul_f32 v[56:57], v[56:57], v[204:205]
	v_pk_mul_f32 v[62:63], v[154:155], v[62:63]
	v_pk_mul_f32 v[64:65], v[156:157], v[64:65]
	v_cvt_pk_bf16_f32 v148, v54, v55
	v_cvt_pk_bf16_f32 v176, v62, v63
	v_cvt_pk_bf16_f32 v149, v56, v57
	v_cvt_pk_bf16_f32 v177, v64, v65
	v_pk_fma_f32 v[50:51], v[50:51], v[158:159], v[172:173]
	v_pk_fma_f32 v[52:53], v[52:53], v[158:159], v[174:175]
	v_pk_fma_f32 v[58:59], v[58:59], v[158:159], v[164:165]
	v_pk_fma_f32 v[60:61], v[60:61], v[158:159], v[166:167]
	v_exp_f32_e32 v50, v50
	v_exp_f32_e32 v51, v51
	v_exp_f32_e32 v52, v52
	v_exp_f32_e32 v53, v53
	v_exp_f32_e32 v58, v58
	v_exp_f32_e32 v59, v59
	v_exp_f32_e32 v60, v60
	v_exp_f32_e32 v61, v61
	v_pk_add_f32 v[50:51], v[50:51], 1.0 op_sel_hi:[1,0]
	v_pk_add_f32 v[52:53], v[52:53], 1.0 op_sel_hi:[1,0]
	v_pk_add_f32 v[58:59], v[58:59], 1.0 op_sel_hi:[1,0]
	v_pk_add_f32 v[60:61], v[60:61], 1.0 op_sel_hi:[1,0]
	v_rcp_f32_e32 v50, v50
	v_rcp_f32_e32 v51, v51
	v_rcp_f32_e32 v52, v52
	v_rcp_f32_e32 v53, v53
	v_rcp_f32_e32 v58, v58
	v_rcp_f32_e32 v59, v59
	v_rcp_f32_e32 v60, v60
	v_rcp_f32_e32 v61, v61
	v_pk_mul_f32 v[154:155], v[50:51], v[214:215]
	v_pk_mul_f32 v[156:157], v[52:53], v[216:217]
	v_exp_f32_e32 v154, v154
	v_exp_f32_e32 v155, v155
	v_exp_f32_e32 v156, v156
	v_exp_f32_e32 v157, v157
	v_lshlrev_b32_e32 v224, 16, v130
	v_and_b32_e32 v225, 0xffff0000, v130
	v_lshlrev_b32_e32 v226, 16, v131
	v_and_b32_e32 v227, 0xffff0000, v131
	v_pk_add_f32 v[154:155], v[154:155], 1.0 op_sel_hi:[1,0] neg_lo:[1,0] neg_hi:[1,0]
	v_pk_add_f32 v[156:157], v[156:157], 1.0 op_sel_hi:[1,0] neg_lo:[1,0] neg_hi:[1,0]
	v_sqrt_f32_e32 v154, v154
	v_sqrt_f32_e32 v155, v155
	v_sqrt_f32_e32 v156, v156
	v_sqrt_f32_e32 v157, v157
	v_pk_mul_f32 v[58:59], v[58:59], v[224:225]
	v_pk_mul_f32 v[60:61], v[60:61], v[226:227]
	v_pk_mul_f32 v[50:51], v[50:51], v[206:207]
	v_pk_mul_f32 v[52:53], v[52:53], v[208:209]
	v_pk_mul_f32 v[58:59], v[154:155], v[58:59]
	v_pk_mul_f32 v[60:61], v[156:157], v[60:61]
	v_cvt_pk_bf16_f32 v150, v50, v51
	v_cvt_pk_bf16_f32 v178, v58, v59
	v_cvt_pk_bf16_f32 v151, v52, v53
	v_cvt_pk_bf16_f32 v179, v60, v61
	global_store_dwordx4 v195, v[148:151], s[42:43]
	global_store_dwordx4 v195, v[176:179], s[40:41]
	v_add_u32_e32 v195, 0x8000, v195
	s_waitcnt vmcnt(12)
	v_pk_fma_f32 v[38:39], v[38:39], v[158:159], v[168:169]
	v_pk_fma_f32 v[40:41], v[40:41], v[158:159], v[170:171]
	v_pk_fma_f32 v[46:47], v[46:47], v[158:159], v[160:161]
	v_pk_fma_f32 v[48:49], v[48:49], v[158:159], v[162:163]
	v_exp_f32_e32 v38, v38
	v_exp_f32_e32 v39, v39
	v_exp_f32_e32 v40, v40
	v_exp_f32_e32 v41, v41
	v_exp_f32_e32 v46, v46
	v_exp_f32_e32 v47, v47
	v_exp_f32_e32 v48, v48
	v_exp_f32_e32 v49, v49
	v_pk_add_f32 v[38:39], v[38:39], 1.0 op_sel_hi:[1,0]
	v_pk_add_f32 v[40:41], v[40:41], 1.0 op_sel_hi:[1,0]
	v_pk_add_f32 v[46:47], v[46:47], 1.0 op_sel_hi:[1,0]
	v_pk_add_f32 v[48:49], v[48:49], 1.0 op_sel_hi:[1,0]
	v_rcp_f32_e32 v38, v38
	v_rcp_f32_e32 v39, v39
	v_rcp_f32_e32 v40, v40
	v_rcp_f32_e32 v41, v41
	v_rcp_f32_e32 v46, v46
	v_rcp_f32_e32 v47, v47
	v_rcp_f32_e32 v48, v48
	v_rcp_f32_e32 v49, v49
	v_pk_mul_f32 v[154:155], v[38:39], v[210:211]
	v_pk_mul_f32 v[156:157], v[40:41], v[212:213]
	v_exp_f32_e32 v154, v154
	v_exp_f32_e32 v155, v155
	v_exp_f32_e32 v156, v156
	v_exp_f32_e32 v157, v157
	v_lshlrev_b32_e32 v224, 16, v124
	v_and_b32_e32 v225, 0xffff0000, v124
	v_lshlrev_b32_e32 v226, 16, v125
	v_and_b32_e32 v227, 0xffff0000, v125
	v_pk_add_f32 v[154:155], v[154:155], 1.0 op_sel_hi:[1,0] neg_lo:[1,0] neg_hi:[1,0]
	v_pk_add_f32 v[156:157], v[156:157], 1.0 op_sel_hi:[1,0] neg_lo:[1,0] neg_hi:[1,0]
	v_sqrt_f32_e32 v154, v154
	v_sqrt_f32_e32 v155, v155
	v_sqrt_f32_e32 v156, v156
	v_sqrt_f32_e32 v157, v157
	v_pk_mul_f32 v[46:47], v[46:47], v[224:225]
	v_pk_mul_f32 v[48:49], v[48:49], v[226:227]
	v_pk_mul_f32 v[38:39], v[38:39], v[202:203]
	v_pk_mul_f32 v[40:41], v[40:41], v[204:205]
	v_pk_mul_f32 v[46:47], v[154:155], v[46:47]
	v_pk_mul_f32 v[48:49], v[156:157], v[48:49]
	v_cvt_pk_bf16_f32 v148, v38, v39
	v_cvt_pk_bf16_f32 v176, v46, v47
; __device__ __forceinline__ float bf_lo(unsigned w) { return __uint_as_float(w << 16); }
; __device__ __forceinline__ float bf_hi(unsigned w) { return __uint_as_float(w & 0xffff0000u); }
; __device__ __forceinline__ void store_bf16x8(bf16* p, const f32x4 v0, const f32x4 v1) { u32x4 w; w.x = cvt_pk_bf16(v0[0], v0[1]); w.y = cvt_pk_bf16(v0[2], v0[3]); w.z = cvt_pk_bf16(v1[0], v1[1]); w.w = cvt_pk_bf16(v1[2], v1[3]); *(u32x4*)p = w; }
; template <bool FP8>
; __device__ __forceinline__ void epilogue(const Desc& d, const Acc& acc, const Tile& u, LAS unsigned char* lds) {
;     ...
;             for (int m = 0; m < 4; ++m) { const size_t ro = (size_t)(row0 + ai * 128 + m * 16) * D + ch0;
;                 const float uf[2][4] = {{bf_lo(uw[m].x), bf_hi(uw[m].x), bf_lo(uw[m].y), bf_hi(uw[m].y)}, {bf_lo(uw[m].z), bf_hi(uw[m].z), bf_lo(uw[m].w), bf_hi(uw[m].w)}};
;                 f32x4 lo[2], bo[2];
; #pragma unroll
;                 for (int n = 0; n < 2; ++n)
; #pragma unroll
;                     for (int j = 0; j < 4; ++j) {
;                         const float it = __builtin_amdgcn_rcpf(1.f + __builtin_amdgcn_exp2f(__builtin_fmaf(acc[ai][0][m][n][j], -L2E, nbx[n][j])));
;                         const float rt = __builtin_amdgcn_rcpf(1.f + __builtin_amdgcn_exp2f(__builtin_fmaf(acc[ai][1][m][n][j], -L2E, nba[n][j])));
;                         const float em = 1.f - __builtin_amdgcn_exp2f(sp2[n][j] * rt);
;                         lo[n][j] = sp[n][j] * rt; bo[n][j] = __builtin_amdgcn_sqrtf(em) * (it * uf[n][j]); }
;                 store_bf16x8(la + ro, lo[0], lo[1]); store_bf16x8(bb + ro, bo[0], bo[1]); } }
	v_cvt_pk_bf16_f32 v149, v40, v41
	v_cvt_pk_bf16_f32 v177, v48, v49
	v_pk_fma_f32 v[34:35], v[34:35], v[158:159], v[172:173]
	v_pk_fma_f32 v[36:37], v[36:37], v[158:159], v[174:175]
	v_pk_fma_f32 v[42:43], v[42:43], v[158:159], v[164:165]
	v_pk_fma_f32 v[44:45], v[44:45], v[158:159], v[166:167]
	v_exp_f32_e32 v34, v34
	v_exp_f32_e32 v35, v35
	v_exp_f32_e32 v36, v36
	v_exp_f32_e32 v37, v37
	v_exp_f32_e32 v42, v42
	v_exp_f32_e32 v43, v43
	v_exp_f32_e32 v44, v44
	v_exp_f32_e32 v45, v45
	v_pk_add_f32 v[34:35], v[34:35], 1.0 op_sel_hi:[1,0]
	v_pk_add_f32 v[36:37], v[36:37], 1.0 op_sel_hi:[1,0]
	v_pk_add_f32 v[42:43], v[42:43], 1.0 op_sel_hi:[1,0]
	v_pk_add_f32 v[44:45], v[44:45], 1.0 op_sel_hi:[1,0]
	v_rcp_f32_e32 v34, v34
	v_rcp_f32_e32 v35, v35
	v_rcp_f32_e32 v36, v36
	v_rcp_f32_e32 v37, v37
	v_rcp_f32_e32 v42, v42
	v_rcp_f32_e32 v43, v43
	v_rcp_f32_e32 v44, v44
	v_rcp_f32_e32 v45, v45
	v_pk_mul_f32 v[154:155], v[34:35], v[214:215]
	v_pk_mul_f32 v[156:157], v[36:37], v[216:217]
	v_exp_f32_e32 v154, v154
	v_exp_f32_e32 v155, v155
	v_exp_f32_e32 v156, v156
	v_exp_f32_e32 v157, v157
	v_lshlrev_b32_e32 v224, 16, v126
	v_and_b32_e32 v225, 0xffff0000, v126
	v_lshlrev_b32_e32 v226, 16, v127
	v_and_b32_e32 v227, 0xffff0000, v127
	v_pk_add_f32 v[154:155], v[154:155], 1.0 op_sel_hi:[1,0] neg_lo:[1,0] neg_hi:[1,0]
	v_pk_add_f32 v[156:157], v[156:157], 1.0 op_sel_hi:[1,0] neg_lo:[1,0] neg_hi:[1,0]
	v_sqrt_f32_e32 v154, v154
	v_sqrt_f32_e32 v155, v155
	v_sqrt_f32_e32 v156, v156
	v_sqrt_f32_e32 v157, v157
	v_pk_mul_f32 v[42:43], v[42:43], v[224:225]
	v_pk_mul_f32 v[44:45], v[44:45], v[226:227]
	v_pk_mul_f32 v[34:35], v[34:35], v[206:207]
	v_pk_mul_f32 v[36:37], v[36:37], v[208:209]
	v_pk_mul_f32 v[42:43], v[154:155], v[42:43]
	v_pk_mul_f32 v[44:45], v[156:157], v[44:45]
	v_cvt_pk_bf16_f32 v150, v34, v35
	v_cvt_pk_bf16_f32 v178, v42, v43
	v_cvt_pk_bf16_f32 v151, v36, v37
	v_cvt_pk_bf16_f32 v179, v44, v45
	global_store_dwordx4 v195, v[148:151], s[42:43]
	global_store_dwordx4 v195, v[176:179], s[40:41]
	v_add_u32_e32 v195, 0x8000, v195
	s_waitcnt vmcnt(13)
	v_pk_fma_f32 v[22:23], v[22:23], v[158:159], v[168:169]
	v_pk_fma_f32 v[24:25], v[24:25], v[158:159], v[170:171]
	v_pk_fma_f32 v[30:31], v[30:31], v[158:159], v[160:161]
	v_pk_fma_f32 v[32:33], v[32:33], v[158:159], v[162:163]
	v_exp_f32_e32 v22, v22
	v_exp_f32_e32 v23, v23
	v_exp_f32_e32 v24, v24
	v_exp_f32_e32 v25, v25
	v_exp_f32_e32 v30, v30
	v_exp_f32_e32 v31, v31
	v_exp_f32_e32 v32, v32
	v_exp_f32_e32 v33, v33
	v_pk_add_f32 v[22:23], v[22:23], 1.0 op_sel_hi:[1,0]
	v_pk_add_f32 v[24:25], v[24:25], 1.0 op_sel_hi:[1,0]
	v_pk_add_f32 v[30:31], v[30:31], 1.0 op_sel_hi:[1,0]
	v_pk_add_f32 v[32:33], v[32:33], 1.0 op_sel_hi:[1,0]
	v_rcp_f32_e32 v22, v22
	v_rcp_f32_e32 v23, v23
	v_rcp_f32_e32 v24, v24
	v_rcp_f32_e32 v25, v25
	v_rcp_f32_e32 v30, v30
	v_rcp_f32_e32 v31, v31
	v_rcp_f32_e32 v32, v32
	v_rcp_f32_e32 v33, v33
	v_pk_mul_f32 v[154:155], v[22:23], v[210:211]
	v_pk_mul_f32 v[156:157], v[24:25], v[212:213]
	v_exp_f32_e32 v154, v154
	v_exp_f32_e32 v155, v155
	v_exp_f32_e32 v156, v156
	v_exp_f32_e32 v157, v157
	v_lshlrev_b32_e32 v224, 16, v120
	v_and_b32_e32 v225, 0xffff0000, v120
	v_lshlrev_b32_e32 v226, 16, v121
	v_and_b32_e32 v227, 0xffff0000, v121
	v_pk_add_f32 v[154:155], v[154:155], 1.0 op_sel_hi:[1,0] neg_lo:[1,0] neg_hi:[1,0]
	v_pk_add_f32 v[156:157], v[156:157], 1.0 op_sel_hi:[1,0] neg_lo:[1,0] neg_hi:[1,0]
	v_sqrt_f32_e32 v154, v154
	v_sqrt_f32_e32 v155, v155
	v_sqrt_f32_e32 v156, v156
	v_sqrt_f32_e32 v157, v157
	v_pk_mul_f32 v[30:31], v[30:31], v[224:225]
	v_pk_mul_f32 v[32:33], v[32:33], v[226:227]
	v_pk_mul_f32 v[22:23], v[22:23], v[202:203]
	v_pk_mul_f32 v[24:25], v[24:25], v[204:205]
	v_pk_mul_f32 v[30:31], v[154:155], v[30:31]
	v_pk_mul_f32 v[32:33], v[156:157], v[32:33]
	v_cvt_pk_bf16_f32 v148, v22, v23
	v_cvt_pk_bf16_f32 v176, v30, v31
	v_cvt_pk_bf16_f32 v149, v24, v25
	v_cvt_pk_bf16_f32 v177, v32, v33
	v_pk_fma_f32 v[18:19], v[18:19], v[158:159], v[172:173]
	v_pk_fma_f32 v[20:21], v[20:21], v[158:159], v[174:175]
	v_pk_fma_f32 v[26:27], v[26:27], v[158:159], v[164:165]
	v_pk_fma_f32 v[28:29], v[28:29], v[158:159], v[166:167]
	v_exp_f32_e32 v18, v18
	v_exp_f32_e32 v19, v19
	v_exp_f32_e32 v20, v20
	v_exp_f32_e32 v21, v21
	v_exp_f32_e32 v26, v26
	v_exp_f32_e32 v27, v27
	v_exp_f32_e32 v28, v28
	v_exp_f32_e32 v29, v29
	v_pk_add_f32 v[18:19], v[18:19], 1.0 op_sel_hi:[1,0]
	v_pk_add_f32 v[20:21], v[20:21], 1.0 op_sel_hi:[1,0]
	v_pk_add_f32 v[26:27], v[26:27], 1.0 op_sel_hi:[1,0]
	v_pk_add_f32 v[28:29], v[28:29], 1.0 op_sel_hi:[1,0]
	v_rcp_f32_e32 v18, v18
	v_rcp_f32_e32 v19, v19
	v_rcp_f32_e32 v20, v20
	v_rcp_f32_e32 v21, v21
	v_rcp_f32_e32 v26, v26
	v_rcp_f32_e32 v27, v27
	v_rcp_f32_e32 v28, v28
	v_rcp_f32_e32 v29, v29
	v_pk_mul_f32 v[154:155], v[18:19], v[214:215]
	v_pk_mul_f32 v[156:157], v[20:21], v[216:217]
	v_exp_f32_e32 v154, v154
	v_exp_f32_e32 v155, v155
	v_exp_f32_e32 v156, v156
	v_exp_f32_e32 v157, v157
	v_lshlrev_b32_e32 v224, 16, v122
	v_and_b32_e32 v225, 0xffff0000, v122
	v_lshlrev_b32_e32 v226, 16, v123
	v_and_b32_e32 v227, 0xffff0000, v123
	v_pk_add_f32 v[154:155], v[154:155], 1.0 op_sel_hi:[1,0] neg_lo:[1,0] neg_hi:[1,0]
	v_pk_add_f32 v[156:157], v[156:157], 1.0 op_sel_hi:[1,0] neg_lo:[1,0] neg_hi:[1,0]
	v_sqrt_f32_e32 v154, v154
	v_sqrt_f32_e32 v155, v155
	v_sqrt_f32_e32 v156, v156
	v_sqrt_f32_e32 v157, v157
	v_pk_mul_f32 v[26:27], v[26:27], v[224:225]
	v_pk_mul_f32 v[28:29], v[28:29], v[226:227]
	v_pk_mul_f32 v[18:19], v[18:19], v[206:207]
	v_pk_mul_f32 v[20:21], v[20:21], v[208:209]
	v_pk_mul_f32 v[26:27], v[154:155], v[26:27]
	v_pk_mul_f32 v[28:29], v[156:157], v[28:29]
	v_cvt_pk_bf16_f32 v150, v18, v19
	v_cvt_pk_bf16_f32 v178, v26, v27
	v_cvt_pk_bf16_f32 v151, v20, v21
	v_cvt_pk_bf16_f32 v179, v28, v29
	global_store_dwordx4 v195, v[148:151], s[42:43]
	global_store_dwordx4 v195, v[176:179], s[40:41]
	v_add_u32_e32 v195, 0x8000, v195
	s_waitcnt vmcnt(14)
; __device__ __forceinline__ float bf_lo(unsigned w) { return __uint_as_float(w << 16); }
; __device__ __forceinline__ float bf_hi(unsigned w) { return __uint_as_float(w & 0xffff0000u); }
; __device__ __forceinline__ void store_bf16x8(bf16* p, const f32x4 v0, const f32x4 v1) { u32x4 w; w.x = cvt_pk_bf16(v0[0], v0[1]); w.y = cvt_pk_bf16(v0[2], v0[3]); w.z = cvt_pk_bf16(v1[0], v1[1]); w.w = cvt_pk_bf16(v1[2], v1[3]); *(u32x4*)p = w; }
; template <bool FP8>
; __device__ __forceinline__ void epilogue(const Desc& d, const Acc& acc, const Tile& u, LAS unsigned char* lds) {
;     ...
;             for (int m = 0; m < 4; ++m) { const size_t ro = (size_t)(row0 + ai * 128 + m * 16) * D + ch0;
;                 const float uf[2][4] = {{bf_lo(uw[m].x), bf_hi(uw[m].x), bf_lo(uw[m].y), bf_hi(uw[m].y)}, {bf_lo(uw[m].z), bf_hi(uw[m].z), bf_lo(uw[m].w), bf_hi(uw[m].w)}};
;                 f32x4 lo[2], bo[2];
; #pragma unroll
;                 for (int n = 0; n < 2; ++n)
; #pragma unroll
;                     for (int j = 0; j < 4; ++j) {
;                         const float it = __builtin_amdgcn_rcpf(1.f + __builtin_amdgcn_exp2f(__builtin_fmaf(acc[ai][0][m][n][j], -L2E, nbx[n][j])));
;                         const float rt = __builtin_amdgcn_rcpf(1.f + __builtin_amdgcn_exp2f(__builtin_fmaf(acc[ai][1][m][n][j], -L2E, nba[n][j])));
;                         const float em = 1.f - __builtin_amdgcn_exp2f(sp2[n][j] * rt);
;                         lo[n][j] = sp[n][j] * rt; bo[n][j] = __builtin_amdgcn_sqrtf(em) * (it * uf[n][j]); }
;                 store_bf16x8(la + ro, lo[0], lo[1]); store_bf16x8(bb + ro, bo[0], bo[1]); } }
	v_pk_fma_f32 v[6:7], v[6:7], v[158:159], v[168:169]
	v_pk_fma_f32 v[8:9], v[8:9], v[158:159], v[170:171]
	v_pk_fma_f32 v[14:15], v[14:15], v[158:159], v[160:161]
	v_pk_fma_f32 v[16:17], v[16:17], v[158:159], v[162:163]
	v_exp_f32_e32 v6, v6
	v_exp_f32_e32 v7, v7
	v_exp_f32_e32 v8, v8
	v_exp_f32_e32 v9, v9
	v_exp_f32_e32 v14, v14
	v_exp_f32_e32 v15, v15
	v_exp_f32_e32 v16, v16
	v_exp_f32_e32 v17, v17
	v_pk_add_f32 v[6:7], v[6:7], 1.0 op_sel_hi:[1,0]
	v_pk_add_f32 v[8:9], v[8:9], 1.0 op_sel_hi:[1,0]
	v_pk_add_f32 v[14:15], v[14:15], 1.0 op_sel_hi:[1,0]
	v_pk_add_f32 v[16:17], v[16:17], 1.0 op_sel_hi:[1,0]
	v_rcp_f32_e32 v6, v6
	v_rcp_f32_e32 v7, v7
	v_rcp_f32_e32 v8, v8
	v_rcp_f32_e32 v9, v9
	v_rcp_f32_e32 v14, v14
	v_rcp_f32_e32 v15, v15
	v_rcp_f32_e32 v16, v16
	v_rcp_f32_e32 v17, v17
	v_pk_mul_f32 v[154:155], v[6:7], v[210:211]
	v_pk_mul_f32 v[156:157], v[8:9], v[212:213]
	v_exp_f32_e32 v154, v154
	v_exp_f32_e32 v155, v155
	v_exp_f32_e32 v156, v156
	v_exp_f32_e32 v157, v157
	v_lshlrev_b32_e32 v224, 16, v116
	v_and_b32_e32 v225, 0xffff0000, v116
	v_lshlrev_b32_e32 v226, 16, v117
	v_and_b32_e32 v227, 0xffff0000, v117
	v_pk_add_f32 v[154:155], v[154:155], 1.0 op_sel_hi:[1,0] neg_lo:[1,0] neg_hi:[1,0]
	v_pk_add_f32 v[156:157], v[156:157], 1.0 op_sel_hi:[1,0] neg_lo:[1,0] neg_hi:[1,0]
	v_sqrt_f32_e32 v154, v154
	v_sqrt_f32_e32 v155, v155
	v_sqrt_f32_e32 v156, v156
	v_sqrt_f32_e32 v157, v157
	v_pk_mul_f32 v[14:15], v[14:15], v[224:225]
	v_pk_mul_f32 v[16:17], v[16:17], v[226:227]
	v_pk_mul_f32 v[6:7], v[6:7], v[202:203]
	v_pk_mul_f32 v[8:9], v[8:9], v[204:205]
	v_pk_mul_f32 v[14:15], v[154:155], v[14:15]
	v_pk_mul_f32 v[16:17], v[156:157], v[16:17]
	v_cvt_pk_bf16_f32 v148, v6, v7
	v_cvt_pk_bf16_f32 v176, v14, v15
	v_cvt_pk_bf16_f32 v149, v8, v9
	v_cvt_pk_bf16_f32 v177, v16, v17
	v_pk_fma_f32 v[2:3], v[2:3], v[158:159], v[172:173]
	v_pk_fma_f32 v[4:5], v[4:5], v[158:159], v[174:175]
	v_pk_fma_f32 v[10:11], v[10:11], v[158:159], v[164:165]
	v_pk_fma_f32 v[12:13], v[12:13], v[158:159], v[166:167]
	v_exp_f32_e32 v2, v2
	v_exp_f32_e32 v3, v3
	v_exp_f32_e32 v4, v4
	v_exp_f32_e32 v5, v5
	v_exp_f32_e32 v10, v10
	v_exp_f32_e32 v11, v11
	v_exp_f32_e32 v12, v12
	v_exp_f32_e32 v13, v13
	v_pk_add_f32 v[2:3], v[2:3], 1.0 op_sel_hi:[1,0]
	v_pk_add_f32 v[4:5], v[4:5], 1.0 op_sel_hi:[1,0]
	v_pk_add_f32 v[10:11], v[10:11], 1.0 op_sel_hi:[1,0]
	v_pk_add_f32 v[12:13], v[12:13], 1.0 op_sel_hi:[1,0]
	v_rcp_f32_e32 v2, v2
	v_rcp_f32_e32 v3, v3
	v_rcp_f32_e32 v4, v4
	v_rcp_f32_e32 v5, v5
	v_rcp_f32_e32 v10, v10
	v_rcp_f32_e32 v11, v11
	v_rcp_f32_e32 v12, v12
	v_rcp_f32_e32 v13, v13
	v_pk_mul_f32 v[154:155], v[2:3], v[214:215]
	v_pk_mul_f32 v[156:157], v[4:5], v[216:217]
	v_exp_f32_e32 v154, v154
	v_exp_f32_e32 v155, v155
	v_exp_f32_e32 v156, v156
	v_exp_f32_e32 v157, v157
	v_lshlrev_b32_e32 v224, 16, v118
	v_and_b32_e32 v225, 0xffff0000, v118
	v_lshlrev_b32_e32 v226, 16, v119
	v_and_b32_e32 v227, 0xffff0000, v119
	v_pk_add_f32 v[154:155], v[154:155], 1.0 op_sel_hi:[1,0] neg_lo:[1,0] neg_hi:[1,0]
	v_pk_add_f32 v[156:157], v[156:157], 1.0 op_sel_hi:[1,0] neg_lo:[1,0] neg_hi:[1,0]
	v_sqrt_f32_e32 v154, v154
	v_sqrt_f32_e32 v155, v155
	v_sqrt_f32_e32 v156, v156
	v_sqrt_f32_e32 v157, v157
	v_pk_mul_f32 v[10:11], v[10:11], v[224:225]
	v_pk_mul_f32 v[12:13], v[12:13], v[226:227]
	v_pk_mul_f32 v[2:3], v[2:3], v[206:207]
	v_pk_mul_f32 v[4:5], v[4:5], v[208:209]
	v_pk_mul_f32 v[10:11], v[154:155], v[10:11]
	v_pk_mul_f32 v[12:13], v[156:157], v[12:13]
	v_cvt_pk_bf16_f32 v150, v2, v3
	v_cvt_pk_bf16_f32 v178, v10, v11
	v_cvt_pk_bf16_f32 v151, v4, v5
	v_cvt_pk_bf16_f32 v179, v12, v13
	global_store_dwordx4 v195, v[148:151], s[42:43]
	global_store_dwordx4 v195, v[176:179], s[40:41]
	s_mov_b64 s[6:7], 0
